# bf16 GEMM epilogues (P2/P6): acc+0.0 packed adds dropped or turned into v_mov_b64
# speedup vs baseline: 1.0141x; 1.0013x over previous
; #define LAS __attribute__((address_space(3)))
; __device__ __forceinline__ unsigned cvt_pk_bf16(float lo, float hi) { unsigned r; asm volatile("v_cvt_pk_bf16_f32 %0, %1, %2" : "=v"(r) : "v"(lo), "v"(hi)); return r; }
;     __device__ __forceinline__ void operator()(const f32x4 (&acc)[2][2][4][2], const Unit& u, int wr, int wc, int fr, int fq) const {
;     ...
; #pragma unroll
;         for (int ai = 0; ai < 2; ++ai)
; #pragma unroll
;             for (int mp = 0; mp < 2; ++mp) {
; #pragma unroll
;                 for (int s = 0; s < 2; ++s)
; #pragma unroll
;                     for (int bj = 0; bj < 2; ++bj) { const int m = 2 * mp + s; const f32x4 v0 = acc[ai][bj][m][0] * scale + bv[bj][0], v1 = acc[ai][bj][m][1] * scale + bv[bj][1];
;                         u32x4 w; w.x = cvt_pk_bf16(v0[0], v0[1]); w.y = cvt_pk_bf16(v0[2], v0[3]); w.z = cvt_pk_bf16(v1[0], v1[1]); w.w = cvt_pk_bf16(v1[2], v1[3]);
;                         *(LAS u32x4*)((s ? wp1 : wp0) + 256 * bj) = w; }
;                 asm volatile("s_waitcnt lgkmcnt(0)" ::: "memory"); __builtin_amdgcn_s_barrier(); asm volatile("" ::: "memory");
;                 bf16_t* g2 = gp + (size_t)(ai * HALF + mp * 32) * ldc;
;                 *(u32x4*)(g2) = *(const LAS u32x4*)(rp0); *(u32x4*)(g2 + HALF) = *(const LAS u32x4*)(rp0 + 256);
.LBB0_329:
	s_nop 7
	s_ashr_i32 s2, s19, 31
	s_lshr_b32 s2, s2, 12
	s_add_i32 s2, s19, s2
	s_and_b32 s2, s2, 0xf00000
	v_lshl_or_b32 v146, s18, 8, v150
	v_mov_b64_e32 v[144:145], s[4:5]
	s_movk_i32 s3, 0x3480
	s_sub_i32 s2, s19, s2
	v_mad_i64_i32 v[144:145], s[18:19], v146, s3, v[144:145]
	v_mov_b64_e32 v[146:147], v[124:125]
	v_mov_b64_e32 v[124:125], v[122:123]
	v_cvt_pk_bf16_f32 v122, v126, v127
	v_cvt_pk_bf16_f32 v123, v128, v129
	v_cvt_pk_bf16_f32 v124, v124, v125
	v_cvt_pk_bf16_f32 v125, v146, v147
	ds_write_b128 v151, v[122:125]
	v_mov_b64_e32 v[122:123], v[112:113]
	v_mov_b64_e32 v[112:113], v[110:111]
	v_cvt_pk_bf16_f32 v110, v118, v119
	v_cvt_pk_bf16_f32 v111, v120, v121
	v_cvt_pk_bf16_f32 v112, v112, v113
	v_cvt_pk_bf16_f32 v113, v122, v123
	ds_write_b128 v151, v[110:113] offset:256
	v_mov_b64_e32 v[110:111], v[116:117]
	v_mov_b64_e32 v[112:113], v[114:115]
	v_mov_b64_e32 v[114:115], v[108:109]
	v_mov_b64_e32 v[108:109], v[106:107]
	v_cvt_pk_bf16_f32 v106, v112, v113
	v_cvt_pk_bf16_f32 v107, v110, v111
	v_cvt_pk_bf16_f32 v108, v108, v109
	v_cvt_pk_bf16_f32 v109, v114, v115
	ds_write_b128 v152, v[106:109] offset:49152
	v_mov_b64_e32 v[106:107], v[100:101]
	v_mov_b64_e32 v[100:101], v[98:99]
	v_cvt_pk_bf16_f32 v98, v102, v103
	v_cvt_pk_bf16_f32 v99, v104, v105
	s_lshl_b32 s2, s2, 8
	v_cvt_pk_bf16_f32 v100, v100, v101
	v_cvt_pk_bf16_f32 v101, v106, v107
	ds_write_b128 v152, v[98:101] offset:49408
	s_waitcnt lgkmcnt(0)
	s_barrier
	ds_read_b128 v[100:103], v153
	ds_read_b128 v[104:107], v153 offset:256
	s_ashr_i32 s3, s2, 31
	v_lshl_add_u64 v[98:99], s[2:3], 1, v[144:145]
	v_lshl_add_u64 v[98:99], v[98:99], 0, v[138:139]
	s_waitcnt lgkmcnt(0)
	global_store_dwordx4 v[98:99], v[100:103], off
	global_store_dwordx4 v[98:99], v[104:107], off offset:256
	ds_read_b128 v[100:103], v154 offset:49152
	ds_read_b128 v[104:107], v154 offset:49408
	s_mov_b32 s2, 0x34000
	v_add_co_u32_e32 v108, vcc, s2, v98
	s_nop 0
	v_addc_co_u32_e32 v109, vcc, 0, v99, vcc
	s_waitcnt lgkmcnt(0)
	global_store_dwordx4 v[108:109], v[100:103], off offset:2048
	global_store_dwordx4 v[108:109], v[104:107], off offset:2304
	s_waitcnt lgkmcnt(0)
	s_barrier
	v_mov_b64_e32 v[100:101], v[92:93]
	v_mov_b64_e32 v[92:93], v[90:91]
	v_cvt_pk_bf16_f32 v90, v94, v95
	v_cvt_pk_bf16_f32 v91, v96, v97
	v_cvt_pk_bf16_f32 v92, v92, v93
	v_cvt_pk_bf16_f32 v93, v100, v101
	ds_write_b128 v151, v[90:93]
	v_mov_b64_e32 v[90:91], v[80:81]
	v_mov_b64_e32 v[80:81], v[78:79]
	v_cvt_pk_bf16_f32 v78, v86, v87
	v_cvt_pk_bf16_f32 v79, v88, v89
	v_cvt_pk_bf16_f32 v80, v80, v81
	v_cvt_pk_bf16_f32 v81, v90, v91
	ds_write_b128 v151, v[78:81] offset:256
	v_mov_b64_e32 v[78:79], v[84:85]
	v_mov_b64_e32 v[80:81], v[82:83]
	v_mov_b64_e32 v[82:83], v[76:77]
	v_mov_b64_e32 v[76:77], v[74:75]
	v_cvt_pk_bf16_f32 v74, v80, v81
	v_cvt_pk_bf16_f32 v75, v78, v79
	v_cvt_pk_bf16_f32 v76, v76, v77
	v_cvt_pk_bf16_f32 v77, v82, v83
	ds_write_b128 v152, v[74:77] offset:49152
	v_mov_b64_e32 v[74:75], v[68:69]
	v_mov_b64_e32 v[68:69], v[66:67]
	v_cvt_pk_bf16_f32 v66, v70, v71
	v_cvt_pk_bf16_f32 v67, v72, v73
	s_mov_b32 s2, 0x69000
	v_cvt_pk_bf16_f32 v68, v68, v69
	v_cvt_pk_bf16_f32 v69, v74, v75
	ds_write_b128 v152, v[66:69] offset:49408
	s_waitcnt lgkmcnt(0)
	s_barrier
	ds_read_b128 v[66:69], v153
	ds_read_b128 v[70:73], v153 offset:256
	v_add_co_u32_e32 v74, vcc, s2, v98
	s_mov_b32 s2, 0x9d000
	s_nop 0
	v_addc_co_u32_e32 v75, vcc, 0, v99, vcc
	s_waitcnt lgkmcnt(0)
	global_store_dwordx4 v[74:75], v[66:69], off
	global_store_dwordx4 v[74:75], v[70:73], off offset:256
	ds_read_b128 v[66:69], v154 offset:49152
	ds_read_b128 v[70:73], v154 offset:49408
	v_add_co_u32_e32 v74, vcc, s2, v98
	s_nop 0
	v_addc_co_u32_e32 v75, vcc, 0, v99, vcc
	s_waitcnt lgkmcnt(0)
	global_store_dwordx4 v[74:75], v[66:69], off offset:2048
	global_store_dwordx4 v[74:75], v[70:73], off offset:2304
	s_waitcnt lgkmcnt(0)
	s_barrier
; #define LAS __attribute__((address_space(3)))
; __device__ __forceinline__ unsigned cvt_pk_bf16(float lo, float hi) { unsigned r; asm volatile("v_cvt_pk_bf16_f32 %0, %1, %2" : "=v"(r) : "v"(lo), "v"(hi)); return r; }
;     __device__ __forceinline__ void operator()(const f32x4 (&acc)[2][2][4][2], const Unit& u, int wr, int wc, int fr, int fq) const {
;     ...
;                     for (int bj = 0; bj < 2; ++bj) { const int m = 2 * mp + s; const f32x4 v0 = acc[ai][bj][m][0] * scale + bv[bj][0], v1 = acc[ai][bj][m][1] * scale + bv[bj][1];
;                         u32x4 w; w.x = cvt_pk_bf16(v0[0], v0[1]); w.y = cvt_pk_bf16(v0[2], v0[3]); w.z = cvt_pk_bf16(v1[0], v1[1]); w.w = cvt_pk_bf16(v1[2], v1[3]);
;                         *(LAS u32x4*)((s ? wp1 : wp0) + 256 * bj) = w; }
;                 asm volatile("s_waitcnt lgkmcnt(0)" ::: "memory"); __builtin_amdgcn_s_barrier(); asm volatile("" ::: "memory");
;                 bf16_t* g2 = gp + (size_t)(ai * HALF + mp * 32) * ldc;
;                 *(u32x4*)(g2) = *(const LAS u32x4*)(rp0); *(u32x4*)(g2 + HALF) = *(const LAS u32x4*)(rp0 + 256);
;                 *(u32x4*)(g2 + (size_t)16 * ldc) = *(const LAS u32x4*)(rp1); *(u32x4*)(g2 + (size_t)16 * ldc + HALF) = *(const LAS u32x4*)(rp1 + 256);
;                 asm volatile("s_waitcnt lgkmcnt(0)" ::: "memory"); __builtin_amdgcn_s_barrier(); asm volatile("" ::: "memory");
;             }
	v_mov_b64_e32 v[66:67], v[60:61]
	v_mov_b64_e32 v[60:61], v[58:59]
	v_cvt_pk_bf16_f32 v58, v62, v63
	v_cvt_pk_bf16_f32 v59, v64, v65
	v_cvt_pk_bf16_f32 v60, v60, v61
	v_cvt_pk_bf16_f32 v61, v66, v67
	ds_write_b128 v151, v[58:61]
	v_mov_b64_e32 v[58:59], v[48:49]
	v_mov_b64_e32 v[48:49], v[46:47]
	v_cvt_pk_bf16_f32 v46, v54, v55
	v_cvt_pk_bf16_f32 v47, v56, v57
	v_cvt_pk_bf16_f32 v48, v48, v49
	v_cvt_pk_bf16_f32 v49, v58, v59
	ds_write_b128 v151, v[46:49] offset:256
	v_mov_b64_e32 v[46:47], v[52:53]
	v_mov_b64_e32 v[48:49], v[50:51]
	v_mov_b64_e32 v[50:51], v[44:45]
	v_mov_b64_e32 v[44:45], v[42:43]
	v_cvt_pk_bf16_f32 v42, v48, v49
	v_cvt_pk_bf16_f32 v43, v46, v47
	v_cvt_pk_bf16_f32 v44, v44, v45
	v_cvt_pk_bf16_f32 v45, v50, v51
	ds_write_b128 v152, v[42:45] offset:49152
	v_mov_b64_e32 v[42:43], v[36:37]
	v_mov_b64_e32 v[36:37], v[34:35]
	v_cvt_pk_bf16_f32 v34, v38, v39
	v_cvt_pk_bf16_f32 v35, v40, v41
	s_mov_b32 s2, 0x1a4000
	v_cvt_pk_bf16_f32 v36, v36, v37
	v_cvt_pk_bf16_f32 v37, v42, v43
	ds_write_b128 v152, v[34:37] offset:49408
	s_waitcnt lgkmcnt(0)
	s_barrier
	ds_read_b128 v[34:37], v153
	ds_read_b128 v[38:41], v153 offset:256
	v_add_co_u32_e32 v42, vcc, s2, v98
	s_mov_b32 s2, 0x1d8000
	s_nop 0
	v_addc_co_u32_e32 v43, vcc, 0, v99, vcc
	s_waitcnt lgkmcnt(0)
	global_store_dwordx4 v[42:43], v[34:37], off
	global_store_dwordx4 v[42:43], v[38:41], off offset:256
	ds_read_b128 v[34:37], v154 offset:49152
	ds_read_b128 v[38:41], v154 offset:49408
	v_add_co_u32_e32 v42, vcc, s2, v98
	s_nop 0
	v_addc_co_u32_e32 v43, vcc, 0, v99, vcc
	s_waitcnt lgkmcnt(0)
	global_store_dwordx4 v[42:43], v[34:37], off offset:2048
	global_store_dwordx4 v[42:43], v[38:41], off offset:2304
	s_waitcnt lgkmcnt(0)
	s_barrier
	v_mov_b64_e32 v[34:35], v[28:29]
	v_mov_b64_e32 v[28:29], v[26:27]
	v_cvt_pk_bf16_f32 v26, v30, v31
	v_cvt_pk_bf16_f32 v27, v32, v33
	v_cvt_pk_bf16_f32 v28, v28, v29
	v_cvt_pk_bf16_f32 v29, v34, v35
	ds_write_b128 v151, v[26:29]
	v_mov_b64_e32 v[26:27], v[16:17]
	v_mov_b64_e32 v[16:17], v[14:15]
	v_cvt_pk_bf16_f32 v14, v22, v23
	v_cvt_pk_bf16_f32 v15, v24, v25
	v_cvt_pk_bf16_f32 v16, v16, v17
	v_cvt_pk_bf16_f32 v17, v26, v27
	ds_write_b128 v151, v[14:17] offset:256
	v_mov_b64_e32 v[14:15], v[20:21]
	v_mov_b64_e32 v[16:17], v[18:19]
	v_mov_b64_e32 v[18:19], v[12:13]
	v_mov_b64_e32 v[12:13], v[10:11]
	v_cvt_pk_bf16_f32 v10, v16, v17
	v_cvt_pk_bf16_f32 v11, v14, v15
	v_cvt_pk_bf16_f32 v12, v12, v13
	v_cvt_pk_bf16_f32 v13, v18, v19
	ds_write_b128 v152, v[10:13] offset:49152
	v_mov_b64_e32 v[10:11], v[4:5]
	v_mov_b64_e32 v[4:5], v[2:3]
	v_cvt_pk_bf16_f32 v2, v6, v7
	v_cvt_pk_bf16_f32 v3, v8, v9
	s_mov_b32 s2, 0x20d000
	v_cvt_pk_bf16_f32 v4, v4, v5
	v_cvt_pk_bf16_f32 v5, v10, v11
	ds_write_b128 v152, v[2:5] offset:49408
	s_waitcnt lgkmcnt(0)
	s_barrier
	ds_read_b128 v[2:5], v153
	ds_read_b128 v[6:9], v153 offset:256
	v_add_co_u32_e32 v10, vcc, s2, v98
	s_cmp_eq_u32 s72, s71
	s_nop 0
	v_addc_co_u32_e32 v11, vcc, 0, v99, vcc
	s_waitcnt lgkmcnt(0)
	global_store_dwordx4 v[10:11], v[2:5], off
	global_store_dwordx4 v[10:11], v[6:9], off offset:256
	ds_read_b128 v[2:5], v154 offset:49152
	ds_read_b128 v[6:9], v154 offset:49408
	v_add_co_u32_e32 v10, vcc, 0x241000, v98
	s_mov_b64 s[2:3], -1
	s_nop 0
	v_addc_co_u32_e32 v11, vcc, 0, v99, vcc
	s_waitcnt lgkmcnt(0)
	global_store_dwordx4 v[10:11], v[2:5], off offset:2048
	global_store_dwordx4 v[10:11], v[6:9], off offset:2304
	s_waitcnt lgkmcnt(0)
	s_barrier
	s_cbranch_scc1 .LBB0_322
	s_andn2_b64 vcc, exec, s[0:1]
	s_cbranch_vccnz .LBB0_321
	s_barrier
	s_branch .LBB0_321

; #define LAS __attribute__((address_space(3)))
; __device__ __forceinline__ unsigned cvt_pk_bf16(float lo, float hi) { unsigned r; asm volatile("v_cvt_pk_bf16_f32 %0, %1, %2" : "=v"(r) : "v"(lo), "v"(hi)); return r; }
;     __device__ __forceinline__ void operator()(const f32x4 (&acc)[2][2][4][2], const Unit& u, int wr, int wc, int fr, int fq) const {
;     ...
; #pragma unroll
;         for (int ai = 0; ai < 2; ++ai)
; #pragma unroll
;             for (int mp = 0; mp < 2; ++mp) {
; #pragma unroll
;                 for (int s = 0; s < 2; ++s)
; #pragma unroll
;                     for (int bj = 0; bj < 2; ++bj) { const int m = 2 * mp + s; const f32x4 v0 = acc[ai][bj][m][0] * scale + bv[bj][0], v1 = acc[ai][bj][m][1] * scale + bv[bj][1];
;                         u32x4 w; w.x = cvt_pk_bf16(v0[0], v0[1]); w.y = cvt_pk_bf16(v0[2], v0[3]); w.z = cvt_pk_bf16(v1[0], v1[1]); w.w = cvt_pk_bf16(v1[2], v1[3]);
;                         *(LAS u32x4*)((s ? wp1 : wp0) + 256 * bj) = w; }
;                 asm volatile("s_waitcnt lgkmcnt(0)" ::: "memory"); __builtin_amdgcn_s_barrier(); asm volatile("" ::: "memory");
;                 bf16_t* g2 = gp + (size_t)(ai * HALF + mp * 32) * ldc;
;                 *(u32x4*)(g2) = *(const LAS u32x4*)(rp0); *(u32x4*)(g2 + HALF) = *(const LAS u32x4*)(rp0 + 256);
.LBB0_724:
	s_nop 7
	v_mov_b64_e32 v[146:147], v[124:125]
	v_mov_b64_e32 v[124:125], v[122:123]
	v_cvt_pk_bf16_f32 v122, v126, v127
	v_cvt_pk_bf16_f32 v123, v128, v129
	v_cvt_pk_bf16_f32 v124, v124, v125
	v_cvt_pk_bf16_f32 v125, v146, v147
	ds_write_b128 v151, v[122:125]
	v_mov_b64_e32 v[122:123], v[112:113]
	v_mov_b64_e32 v[112:113], v[110:111]
	s_ashr_i32 s2, s19, 31
	v_cvt_pk_bf16_f32 v110, v118, v119
	v_cvt_pk_bf16_f32 v111, v120, v121
	v_cvt_pk_bf16_f32 v112, v112, v113
	v_cvt_pk_bf16_f32 v113, v122, v123
	ds_write_b128 v151, v[110:113] offset:256
	v_mov_b64_e32 v[110:111], v[116:117]
	v_mov_b64_e32 v[112:113], v[114:115]
	v_mov_b64_e32 v[114:115], v[108:109]
	v_mov_b64_e32 v[108:109], v[106:107]
	v_cvt_pk_bf16_f32 v106, v112, v113
	v_cvt_pk_bf16_f32 v107, v110, v111
	s_lshr_b32 s2, s2, 12
	v_cvt_pk_bf16_f32 v108, v108, v109
	v_cvt_pk_bf16_f32 v109, v114, v115
	ds_write_b128 v152, v[106:109] offset:49152
	v_mov_b64_e32 v[106:107], v[100:101]
	v_mov_b64_e32 v[100:101], v[98:99]
	s_add_i32 s2, s19, s2
	s_and_b32 s2, s2, 0xf00000
	v_cvt_pk_bf16_f32 v98, v102, v103
	v_cvt_pk_bf16_f32 v99, v104, v105
	v_cvt_pk_bf16_f32 v100, v100, v101
	v_cvt_pk_bf16_f32 v101, v106, v107
	ds_write_b128 v152, v[98:101] offset:49408
	v_lshl_or_b32 v144, s18, 8, v150
	s_waitcnt lgkmcnt(0)
	s_barrier
	s_sub_i32 s2, s19, s2
	v_ashrrev_i32_e32 v145, 31, v144
	ds_read_b128 v[100:103], v153
	ds_read_b128 v[104:107], v153 offset:256
	s_lshl_b32 s2, s2, 8
	v_lshlrev_b64 v[144:145], 12, v[144:145]
	v_lshl_add_u64 v[144:145], s[4:5], 0, v[144:145]
	s_ashr_i32 s3, s2, 31
	v_lshl_add_u64 v[98:99], s[2:3], 1, v[144:145]
	v_lshl_add_u64 v[98:99], v[98:99], 0, v[138:139]
	s_waitcnt lgkmcnt(0)
	global_store_dwordx4 v[98:99], v[100:103], off
	global_store_dwordx4 v[98:99], v[104:107], off offset:256
	ds_read_b128 v[100:103], v154 offset:49152
	ds_read_b128 v[104:107], v154 offset:49408
	v_add_co_u32_e32 v108, vcc, s53, v98
	s_nop 0
	v_addc_co_u32_e32 v109, vcc, 0, v99, vcc
	s_waitcnt lgkmcnt(0)
	global_store_dwordx4 v[108:109], v[100:103], off
	global_store_dwordx4 v[108:109], v[104:107], off offset:256
	s_waitcnt lgkmcnt(0)
	s_barrier
	v_mov_b64_e32 v[100:101], v[92:93]
	v_mov_b64_e32 v[92:93], v[90:91]
	v_cvt_pk_bf16_f32 v90, v94, v95
	v_cvt_pk_bf16_f32 v91, v96, v97
	v_cvt_pk_bf16_f32 v92, v92, v93
	v_cvt_pk_bf16_f32 v93, v100, v101
	ds_write_b128 v151, v[90:93]
	v_mov_b64_e32 v[90:91], v[80:81]
	v_mov_b64_e32 v[80:81], v[78:79]
	v_cvt_pk_bf16_f32 v78, v86, v87
	v_cvt_pk_bf16_f32 v79, v88, v89
	v_cvt_pk_bf16_f32 v80, v80, v81
	v_cvt_pk_bf16_f32 v81, v90, v91
	ds_write_b128 v151, v[78:81] offset:256
	v_mov_b64_e32 v[78:79], v[84:85]
	v_mov_b64_e32 v[80:81], v[82:83]
	v_mov_b64_e32 v[82:83], v[76:77]
	v_mov_b64_e32 v[76:77], v[74:75]
	v_cvt_pk_bf16_f32 v74, v80, v81
	v_cvt_pk_bf16_f32 v75, v78, v79
	v_cvt_pk_bf16_f32 v76, v76, v77
	v_cvt_pk_bf16_f32 v77, v82, v83
	ds_write_b128 v152, v[74:77] offset:49152
	v_mov_b64_e32 v[74:75], v[68:69]
	v_mov_b64_e32 v[68:69], v[66:67]
	v_cvt_pk_bf16_f32 v66, v70, v71
	v_cvt_pk_bf16_f32 v67, v72, v73
	v_cvt_pk_bf16_f32 v68, v68, v69
	v_cvt_pk_bf16_f32 v69, v74, v75
	ds_write_b128 v152, v[66:69] offset:49408
	s_waitcnt lgkmcnt(0)
	s_barrier
	ds_read_b128 v[66:69], v153
	ds_read_b128 v[70:73], v153 offset:256
	v_add_co_u32_e32 v74, vcc, s54, v98
	s_nop 0
	v_addc_co_u32_e32 v75, vcc, 0, v99, vcc
	s_waitcnt lgkmcnt(0)
	global_store_dwordx4 v[74:75], v[66:69], off
	global_store_dwordx4 v[74:75], v[70:73], off offset:256
	ds_read_b128 v[66:69], v154 offset:49152
	ds_read_b128 v[70:73], v154 offset:49408
	v_add_co_u32_e32 v74, vcc, s52, v98
	s_nop 0
	v_addc_co_u32_e32 v75, vcc, 0, v99, vcc
	s_waitcnt lgkmcnt(0)
	global_store_dwordx4 v[74:75], v[66:69], off
	global_store_dwordx4 v[74:75], v[70:73], off offset:256
	s_waitcnt lgkmcnt(0)
	s_barrier
; #define LAS __attribute__((address_space(3)))
; __device__ __forceinline__ unsigned cvt_pk_bf16(float lo, float hi) { unsigned r; asm volatile("v_cvt_pk_bf16_f32 %0, %1, %2" : "=v"(r) : "v"(lo), "v"(hi)); return r; }
;     __device__ __forceinline__ void operator()(const f32x4 (&acc)[2][2][4][2], const Unit& u, int wr, int wc, int fr, int fq) const {
;     ...
;                     for (int bj = 0; bj < 2; ++bj) { const int m = 2 * mp + s; const f32x4 v0 = acc[ai][bj][m][0] * scale + bv[bj][0], v1 = acc[ai][bj][m][1] * scale + bv[bj][1];
;                         u32x4 w; w.x = cvt_pk_bf16(v0[0], v0[1]); w.y = cvt_pk_bf16(v0[2], v0[3]); w.z = cvt_pk_bf16(v1[0], v1[1]); w.w = cvt_pk_bf16(v1[2], v1[3]);
;                         *(LAS u32x4*)((s ? wp1 : wp0) + 256 * bj) = w; }
;                 asm volatile("s_waitcnt lgkmcnt(0)" ::: "memory"); __builtin_amdgcn_s_barrier(); asm volatile("" ::: "memory");
;                 bf16_t* g2 = gp + (size_t)(ai * HALF + mp * 32) * ldc;
;                 *(u32x4*)(g2) = *(const LAS u32x4*)(rp0); *(u32x4*)(g2 + HALF) = *(const LAS u32x4*)(rp0 + 256);
;                 *(u32x4*)(g2 + (size_t)16 * ldc) = *(const LAS u32x4*)(rp1); *(u32x4*)(g2 + (size_t)16 * ldc + HALF) = *(const LAS u32x4*)(rp1 + 256);
;                 asm volatile("s_waitcnt lgkmcnt(0)" ::: "memory"); __builtin_amdgcn_s_barrier(); asm volatile("" ::: "memory");
	v_mov_b64_e32 v[66:67], v[60:61]
	v_mov_b64_e32 v[60:61], v[58:59]
	v_cvt_pk_bf16_f32 v58, v62, v63
	v_cvt_pk_bf16_f32 v59, v64, v65
	v_cvt_pk_bf16_f32 v60, v60, v61
	v_cvt_pk_bf16_f32 v61, v66, v67
	ds_write_b128 v151, v[58:61]
	v_mov_b64_e32 v[58:59], v[48:49]
	v_mov_b64_e32 v[48:49], v[46:47]
	v_cvt_pk_bf16_f32 v46, v54, v55
	v_cvt_pk_bf16_f32 v47, v56, v57
	v_cvt_pk_bf16_f32 v48, v48, v49
	v_cvt_pk_bf16_f32 v49, v58, v59
	ds_write_b128 v151, v[46:49] offset:256
	v_mov_b64_e32 v[46:47], v[52:53]
	v_mov_b64_e32 v[48:49], v[50:51]
	v_mov_b64_e32 v[50:51], v[44:45]
	v_mov_b64_e32 v[44:45], v[42:43]
	v_cvt_pk_bf16_f32 v42, v48, v49
	v_cvt_pk_bf16_f32 v43, v46, v47
	v_cvt_pk_bf16_f32 v44, v44, v45
	v_cvt_pk_bf16_f32 v45, v50, v51
	ds_write_b128 v152, v[42:45] offset:49152
	v_mov_b64_e32 v[42:43], v[36:37]
	v_mov_b64_e32 v[36:37], v[34:35]
	v_cvt_pk_bf16_f32 v34, v38, v39
	v_cvt_pk_bf16_f32 v35, v40, v41
	v_cvt_pk_bf16_f32 v36, v36, v37
	v_cvt_pk_bf16_f32 v37, v42, v43
	ds_write_b128 v152, v[34:37] offset:49408
	s_waitcnt lgkmcnt(0)
	s_barrier
	ds_read_b128 v[34:37], v153
	ds_read_b128 v[38:41], v153 offset:256
	v_add_co_u32_e32 v42, vcc, s55, v98
	s_nop 0
	v_addc_co_u32_e32 v43, vcc, 0, v99, vcc
	s_waitcnt lgkmcnt(0)
	global_store_dwordx4 v[42:43], v[34:37], off
	global_store_dwordx4 v[42:43], v[38:41], off offset:256
	ds_read_b128 v[34:37], v154 offset:49152
	ds_read_b128 v[38:41], v154 offset:49408
	v_add_co_u32_e32 v42, vcc, s56, v98
	s_nop 0
	v_addc_co_u32_e32 v43, vcc, 0, v99, vcc
	s_waitcnt lgkmcnt(0)
	global_store_dwordx4 v[42:43], v[34:37], off
	global_store_dwordx4 v[42:43], v[38:41], off offset:256
	s_waitcnt lgkmcnt(0)
	s_barrier
	v_mov_b64_e32 v[34:35], v[28:29]
	v_mov_b64_e32 v[28:29], v[26:27]
	v_cvt_pk_bf16_f32 v26, v30, v31
	v_cvt_pk_bf16_f32 v27, v32, v33
	v_cvt_pk_bf16_f32 v28, v28, v29
	v_cvt_pk_bf16_f32 v29, v34, v35
	ds_write_b128 v151, v[26:29]
	v_mov_b64_e32 v[26:27], v[16:17]
	v_mov_b64_e32 v[16:17], v[14:15]
	v_cvt_pk_bf16_f32 v14, v22, v23
	v_cvt_pk_bf16_f32 v15, v24, v25
	v_cvt_pk_bf16_f32 v16, v16, v17
	v_cvt_pk_bf16_f32 v17, v26, v27
	ds_write_b128 v151, v[14:17] offset:256
	v_mov_b64_e32 v[14:15], v[20:21]
	v_mov_b64_e32 v[16:17], v[18:19]
	v_mov_b64_e32 v[18:19], v[12:13]
	v_mov_b64_e32 v[12:13], v[10:11]
	v_cvt_pk_bf16_f32 v10, v16, v17
	v_cvt_pk_bf16_f32 v11, v14, v15
	v_cvt_pk_bf16_f32 v12, v12, v13
	v_cvt_pk_bf16_f32 v13, v18, v19
	ds_write_b128 v152, v[10:13] offset:49152
	v_mov_b64_e32 v[10:11], v[4:5]
	v_mov_b64_e32 v[4:5], v[2:3]
	v_cvt_pk_bf16_f32 v2, v6, v7
	v_cvt_pk_bf16_f32 v3, v8, v9
	s_cmp_eq_u32 s51, s50
	v_cvt_pk_bf16_f32 v4, v4, v5
	v_cvt_pk_bf16_f32 v5, v10, v11
	ds_write_b128 v152, v[2:5] offset:49408
	s_waitcnt lgkmcnt(0)
	s_barrier
	ds_read_b128 v[2:5], v153
	ds_read_b128 v[6:9], v153 offset:256
	v_add_co_u32_e32 v10, vcc, s57, v98
	s_mov_b64 s[2:3], -1
	s_nop 0
	v_addc_co_u32_e32 v11, vcc, 0, v99, vcc
	s_waitcnt lgkmcnt(0)
	global_store_dwordx4 v[10:11], v[2:5], off
	global_store_dwordx4 v[10:11], v[6:9], off offset:256
	ds_read_b128 v[2:5], v154 offset:49152
	ds_read_b128 v[6:9], v154 offset:49408
	v_add_co_u32_e32 v10, vcc, 0xb0000, v98
	s_nop 1
	v_addc_co_u32_e32 v11, vcc, 0, v99, vcc
	s_waitcnt lgkmcnt(0)
	global_store_dwordx4 v[10:11], v[2:5], off
	global_store_dwordx4 v[10:11], v[6:9], off offset:256
	s_waitcnt lgkmcnt(0)
	s_barrier
	s_cbranch_scc1 .LBB0_717
	s_andn2_b64 vcc, exec, s[0:1]
	s_cbranch_vccnz .LBB0_716
	s_barrier
	s_branch .LBB0_716
